# loop-edge edit: exact-hit branch test dropped from the first eight bisection passes of the top-256 selection
# speedup vs baseline: 1.0014x; 1.0014x over previous
.Lmy_s1_p0:
	v_and_b32_e32 v50, v10, v91
	v_bcnt_u32_b32 v52, v50, v14
	s_nop 1
	v_add_u32_dpp v53, v52, v52 quad_perm:[1,0,3,2] row_mask:0xf bank_mask:0xf bound_ctrl:1
	s_nop 1
	v_add_u32_dpp v53, v53, v53 quad_perm:[2,3,0,1] row_mask:0xf bank_mask:0xf bound_ctrl:1
	s_nop 1
	v_add_u32_dpp v53, v53, v53 row_half_mirror row_mask:0xf bank_mask:0xf bound_ctrl:1
	s_nop 1
	v_add_u32_dpp v53, v53, v53 row_mirror row_mask:0xf bank_mask:0xf bound_ctrl:1
	v_mov_b32_e32 v54, v53
	s_nop 1
	v_permlane16_swap_b32 v53, v54
	v_add_u32_e32 v53, v53, v54
	v_cmp_gt_i32_e32 vcc, 0x100, v53
	s_nop 0
	s_nop 0
	v_cndmask_b32_e64 v55, 0, -1, vcc
	v_cndmask_b32_e32 v14, v14, v52, vcc
	v_bitop3_b32 v12, v12, v50, v55 bitop3:0xf8
	v_bitop3_b32 v10, v10, v91, v55 bitop3:0x60
.Lmy_s1_p1:
	v_and_b32_e32 v50, v10, v62
	v_bcnt_u32_b32 v52, v50, v14
	s_nop 1
	v_add_u32_dpp v53, v52, v52 quad_perm:[1,0,3,2] row_mask:0xf bank_mask:0xf bound_ctrl:1
	s_nop 1
	v_add_u32_dpp v53, v53, v53 quad_perm:[2,3,0,1] row_mask:0xf bank_mask:0xf bound_ctrl:1
	s_nop 1
	v_add_u32_dpp v53, v53, v53 row_half_mirror row_mask:0xf bank_mask:0xf bound_ctrl:1
	s_nop 1
	v_add_u32_dpp v53, v53, v53 row_mirror row_mask:0xf bank_mask:0xf bound_ctrl:1
	v_mov_b32_e32 v54, v53
	s_nop 1
	v_permlane16_swap_b32 v53, v54
	v_add_u32_e32 v53, v53, v54
	v_cmp_gt_i32_e32 vcc, 0x100, v53
	s_nop 0
	s_nop 0
	v_cndmask_b32_e64 v55, 0, -1, vcc
	v_cndmask_b32_e32 v14, v14, v52, vcc
	v_bitop3_b32 v12, v12, v50, v55 bitop3:0xf8
	v_bitop3_b32 v10, v10, v62, v55 bitop3:0x60
.Lmy_s1_p2:
	v_and_b32_e32 v50, v10, v76
	v_bcnt_u32_b32 v52, v50, v14
	s_nop 1
	v_add_u32_dpp v53, v52, v52 quad_perm:[1,0,3,2] row_mask:0xf bank_mask:0xf bound_ctrl:1
	s_nop 1
	v_add_u32_dpp v53, v53, v53 quad_perm:[2,3,0,1] row_mask:0xf bank_mask:0xf bound_ctrl:1
	s_nop 1
	v_add_u32_dpp v53, v53, v53 row_half_mirror row_mask:0xf bank_mask:0xf bound_ctrl:1
	s_nop 1
	v_add_u32_dpp v53, v53, v53 row_mirror row_mask:0xf bank_mask:0xf bound_ctrl:1
	v_mov_b32_e32 v54, v53
	s_nop 1
	v_permlane16_swap_b32 v53, v54
	v_add_u32_e32 v53, v53, v54
	v_cmp_gt_i32_e32 vcc, 0x100, v53
	s_nop 0
	s_nop 0
	v_cndmask_b32_e64 v55, 0, -1, vcc
	v_cndmask_b32_e32 v14, v14, v52, vcc
	v_bitop3_b32 v12, v12, v50, v55 bitop3:0xf8
	v_bitop3_b32 v10, v10, v76, v55 bitop3:0x60
.Lmy_s1_p3:
	v_and_b32_e32 v50, v10, v77
	v_bcnt_u32_b32 v52, v50, v14
	s_nop 1
	v_add_u32_dpp v53, v52, v52 quad_perm:[1,0,3,2] row_mask:0xf bank_mask:0xf bound_ctrl:1
	s_nop 1
	v_add_u32_dpp v53, v53, v53 quad_perm:[2,3,0,1] row_mask:0xf bank_mask:0xf bound_ctrl:1
	s_nop 1
	v_add_u32_dpp v53, v53, v53 row_half_mirror row_mask:0xf bank_mask:0xf bound_ctrl:1
	s_nop 1
	v_add_u32_dpp v53, v53, v53 row_mirror row_mask:0xf bank_mask:0xf bound_ctrl:1
	v_mov_b32_e32 v54, v53
	s_nop 1
	v_permlane16_swap_b32 v53, v54
	v_add_u32_e32 v53, v53, v54
	v_cmp_gt_i32_e32 vcc, 0x100, v53
	s_nop 0
	s_nop 0
	v_cndmask_b32_e64 v55, 0, -1, vcc
	v_cndmask_b32_e32 v14, v14, v52, vcc
	v_bitop3_b32 v12, v12, v50, v55 bitop3:0xf8
	v_bitop3_b32 v10, v10, v77, v55 bitop3:0x60
.Lmy_s1_p4:
	v_and_b32_e32 v50, v10, v78
	v_bcnt_u32_b32 v52, v50, v14
	s_nop 1
	v_add_u32_dpp v53, v52, v52 quad_perm:[1,0,3,2] row_mask:0xf bank_mask:0xf bound_ctrl:1
	s_nop 1
	v_add_u32_dpp v53, v53, v53 quad_perm:[2,3,0,1] row_mask:0xf bank_mask:0xf bound_ctrl:1
	s_nop 1
	v_add_u32_dpp v53, v53, v53 row_half_mirror row_mask:0xf bank_mask:0xf bound_ctrl:1
	s_nop 1
	v_add_u32_dpp v53, v53, v53 row_mirror row_mask:0xf bank_mask:0xf bound_ctrl:1
	v_mov_b32_e32 v54, v53
	s_nop 1
	v_permlane16_swap_b32 v53, v54
	v_add_u32_e32 v53, v53, v54
	v_cmp_gt_i32_e32 vcc, 0x100, v53
	s_nop 0
	s_nop 0
	v_cndmask_b32_e64 v55, 0, -1, vcc
	v_cndmask_b32_e32 v14, v14, v52, vcc
	v_bitop3_b32 v12, v12, v50, v55 bitop3:0xf8
	v_bitop3_b32 v10, v10, v78, v55 bitop3:0x60
.Lmy_s1_p5:
	v_and_b32_e32 v50, v10, v79
	v_bcnt_u32_b32 v52, v50, v14
	s_nop 1
	v_add_u32_dpp v53, v52, v52 quad_perm:[1,0,3,2] row_mask:0xf bank_mask:0xf bound_ctrl:1
	s_nop 1
	v_add_u32_dpp v53, v53, v53 quad_perm:[2,3,0,1] row_mask:0xf bank_mask:0xf bound_ctrl:1
	s_nop 1
	v_add_u32_dpp v53, v53, v53 row_half_mirror row_mask:0xf bank_mask:0xf bound_ctrl:1
	s_nop 1
	v_add_u32_dpp v53, v53, v53 row_mirror row_mask:0xf bank_mask:0xf bound_ctrl:1
	v_mov_b32_e32 v54, v53
	s_nop 1
	v_permlane16_swap_b32 v53, v54
	v_add_u32_e32 v53, v53, v54
	v_cmp_gt_i32_e32 vcc, 0x100, v53
	s_nop 0
	s_nop 0
	v_cndmask_b32_e64 v55, 0, -1, vcc
	v_cndmask_b32_e32 v14, v14, v52, vcc
	v_bitop3_b32 v12, v12, v50, v55 bitop3:0xf8
	v_bitop3_b32 v10, v10, v79, v55 bitop3:0x60
.Lmy_s1_p6:
	v_and_b32_e32 v50, v10, v80
	v_bcnt_u32_b32 v52, v50, v14
	s_nop 1
	v_add_u32_dpp v53, v52, v52 quad_perm:[1,0,3,2] row_mask:0xf bank_mask:0xf bound_ctrl:1
	s_nop 1
	v_add_u32_dpp v53, v53, v53 quad_perm:[2,3,0,1] row_mask:0xf bank_mask:0xf bound_ctrl:1
	s_nop 1
	v_add_u32_dpp v53, v53, v53 row_half_mirror row_mask:0xf bank_mask:0xf bound_ctrl:1
	s_nop 1
	v_add_u32_dpp v53, v53, v53 row_mirror row_mask:0xf bank_mask:0xf bound_ctrl:1
	v_mov_b32_e32 v54, v53
	s_nop 1
	v_permlane16_swap_b32 v53, v54
	v_add_u32_e32 v53, v53, v54
	v_cmp_gt_i32_e32 vcc, 0x100, v53
	s_nop 0
	s_nop 0
	v_cndmask_b32_e64 v55, 0, -1, vcc
	v_cndmask_b32_e32 v14, v14, v52, vcc
	v_bitop3_b32 v12, v12, v50, v55 bitop3:0xf8
	v_bitop3_b32 v10, v10, v80, v55 bitop3:0x60
.Lmy_s1_p7:
	v_and_b32_e32 v50, v10, v81
	v_bcnt_u32_b32 v52, v50, v14
	s_nop 1
	v_add_u32_dpp v53, v52, v52 quad_perm:[1,0,3,2] row_mask:0xf bank_mask:0xf bound_ctrl:1
	s_nop 1
	v_add_u32_dpp v53, v53, v53 quad_perm:[2,3,0,1] row_mask:0xf bank_mask:0xf bound_ctrl:1
	s_nop 1
	v_add_u32_dpp v53, v53, v53 row_half_mirror row_mask:0xf bank_mask:0xf bound_ctrl:1
	s_nop 1
	v_add_u32_dpp v53, v53, v53 row_mirror row_mask:0xf bank_mask:0xf bound_ctrl:1
	v_mov_b32_e32 v54, v53
	s_nop 1
	v_permlane16_swap_b32 v53, v54
	v_add_u32_e32 v53, v53, v54
	v_cmp_gt_i32_e32 vcc, 0x100, v53
	s_nop 0
	s_nop 0
	v_cndmask_b32_e64 v55, 0, -1, vcc
	v_cndmask_b32_e32 v14, v14, v52, vcc
	v_bitop3_b32 v12, v12, v50, v55 bitop3:0xf8
	v_bitop3_b32 v10, v10, v81, v55 bitop3:0x60

.Lmy_s2_p0:
	v_and_b32_e32 v50, v10, v91
	v_and_b32_e32 v51, v11, v123
	v_bcnt_u32_b32 v52, v50, v14
	v_bcnt_u32_b32 v52, v51, v52
	s_nop 1
	v_add_u32_dpp v53, v52, v52 quad_perm:[1,0,3,2] row_mask:0xf bank_mask:0xf bound_ctrl:1
	s_nop 1
	v_add_u32_dpp v53, v53, v53 quad_perm:[2,3,0,1] row_mask:0xf bank_mask:0xf bound_ctrl:1
	s_nop 1
	v_add_u32_dpp v53, v53, v53 row_half_mirror row_mask:0xf bank_mask:0xf bound_ctrl:1
	s_nop 1
	v_add_u32_dpp v53, v53, v53 row_mirror row_mask:0xf bank_mask:0xf bound_ctrl:1
	v_mov_b32_e32 v54, v53
	s_nop 1
	v_permlane16_swap_b32 v53, v54
	v_add_u32_e32 v53, v53, v54
	v_cmp_gt_i32_e32 vcc, 0x100, v53
	s_nop 0
	s_nop 0
	v_cndmask_b32_e64 v55, 0, -1, vcc
	v_cndmask_b32_e32 v14, v14, v52, vcc
	v_bitop3_b32 v12, v12, v50, v55 bitop3:0xf8
	v_bitop3_b32 v13, v13, v51, v55 bitop3:0xf8
	v_bitop3_b32 v10, v10, v91, v55 bitop3:0x60
	v_bitop3_b32 v11, v11, v123, v55 bitop3:0x60
.Lmy_s2_p1:
	v_and_b32_e32 v50, v10, v62
	v_and_b32_e32 v51, v11, v63
	v_bcnt_u32_b32 v52, v50, v14
	v_bcnt_u32_b32 v52, v51, v52
	s_nop 1
	v_add_u32_dpp v53, v52, v52 quad_perm:[1,0,3,2] row_mask:0xf bank_mask:0xf bound_ctrl:1
	s_nop 1
	v_add_u32_dpp v53, v53, v53 quad_perm:[2,3,0,1] row_mask:0xf bank_mask:0xf bound_ctrl:1
	s_nop 1
	v_add_u32_dpp v53, v53, v53 row_half_mirror row_mask:0xf bank_mask:0xf bound_ctrl:1
	s_nop 1
	v_add_u32_dpp v53, v53, v53 row_mirror row_mask:0xf bank_mask:0xf bound_ctrl:1
	v_mov_b32_e32 v54, v53
	s_nop 1
	v_permlane16_swap_b32 v53, v54
	v_add_u32_e32 v53, v53, v54
	v_cmp_gt_i32_e32 vcc, 0x100, v53
	s_nop 0
	s_nop 0
	v_cndmask_b32_e64 v55, 0, -1, vcc
	v_cndmask_b32_e32 v14, v14, v52, vcc
	v_bitop3_b32 v12, v12, v50, v55 bitop3:0xf8
	v_bitop3_b32 v13, v13, v51, v55 bitop3:0xf8
	v_bitop3_b32 v10, v10, v62, v55 bitop3:0x60
	v_bitop3_b32 v11, v11, v63, v55 bitop3:0x60
.Lmy_s2_p2:
	v_and_b32_e32 v50, v10, v76
	v_and_b32_e32 v51, v11, v108
	v_bcnt_u32_b32 v52, v50, v14
	v_bcnt_u32_b32 v52, v51, v52
	s_nop 1
	v_add_u32_dpp v53, v52, v52 quad_perm:[1,0,3,2] row_mask:0xf bank_mask:0xf bound_ctrl:1
	s_nop 1
	v_add_u32_dpp v53, v53, v53 quad_perm:[2,3,0,1] row_mask:0xf bank_mask:0xf bound_ctrl:1
	s_nop 1
	v_add_u32_dpp v53, v53, v53 row_half_mirror row_mask:0xf bank_mask:0xf bound_ctrl:1
	s_nop 1
	v_add_u32_dpp v53, v53, v53 row_mirror row_mask:0xf bank_mask:0xf bound_ctrl:1
	v_mov_b32_e32 v54, v53
	s_nop 1
	v_permlane16_swap_b32 v53, v54
	v_add_u32_e32 v53, v53, v54
	v_cmp_gt_i32_e32 vcc, 0x100, v53
	s_nop 0
	s_nop 0
	v_cndmask_b32_e64 v55, 0, -1, vcc
	v_cndmask_b32_e32 v14, v14, v52, vcc
	v_bitop3_b32 v12, v12, v50, v55 bitop3:0xf8
	v_bitop3_b32 v13, v13, v51, v55 bitop3:0xf8
	v_bitop3_b32 v10, v10, v76, v55 bitop3:0x60
	v_bitop3_b32 v11, v11, v108, v55 bitop3:0x60
.Lmy_s2_p3:
	v_and_b32_e32 v50, v10, v77
	v_and_b32_e32 v51, v11, v109
	v_bcnt_u32_b32 v52, v50, v14
	v_bcnt_u32_b32 v52, v51, v52
	s_nop 1
	v_add_u32_dpp v53, v52, v52 quad_perm:[1,0,3,2] row_mask:0xf bank_mask:0xf bound_ctrl:1
	s_nop 1
	v_add_u32_dpp v53, v53, v53 quad_perm:[2,3,0,1] row_mask:0xf bank_mask:0xf bound_ctrl:1
	s_nop 1
	v_add_u32_dpp v53, v53, v53 row_half_mirror row_mask:0xf bank_mask:0xf bound_ctrl:1
	s_nop 1
	v_add_u32_dpp v53, v53, v53 row_mirror row_mask:0xf bank_mask:0xf bound_ctrl:1
	v_mov_b32_e32 v54, v53
	s_nop 1
	v_permlane16_swap_b32 v53, v54
	v_add_u32_e32 v53, v53, v54
	v_cmp_gt_i32_e32 vcc, 0x100, v53
	s_nop 0
	s_nop 0
	v_cndmask_b32_e64 v55, 0, -1, vcc
	v_cndmask_b32_e32 v14, v14, v52, vcc
	v_bitop3_b32 v12, v12, v50, v55 bitop3:0xf8
	v_bitop3_b32 v13, v13, v51, v55 bitop3:0xf8
	v_bitop3_b32 v10, v10, v77, v55 bitop3:0x60
	v_bitop3_b32 v11, v11, v109, v55 bitop3:0x60
.Lmy_s2_p4:
	v_and_b32_e32 v50, v10, v78
	v_and_b32_e32 v51, v11, v110
	v_bcnt_u32_b32 v52, v50, v14
	v_bcnt_u32_b32 v52, v51, v52
	s_nop 1
	v_add_u32_dpp v53, v52, v52 quad_perm:[1,0,3,2] row_mask:0xf bank_mask:0xf bound_ctrl:1
	s_nop 1
	v_add_u32_dpp v53, v53, v53 quad_perm:[2,3,0,1] row_mask:0xf bank_mask:0xf bound_ctrl:1
	s_nop 1
	v_add_u32_dpp v53, v53, v53 row_half_mirror row_mask:0xf bank_mask:0xf bound_ctrl:1
	s_nop 1
	v_add_u32_dpp v53, v53, v53 row_mirror row_mask:0xf bank_mask:0xf bound_ctrl:1
	v_mov_b32_e32 v54, v53
	s_nop 1
	v_permlane16_swap_b32 v53, v54
	v_add_u32_e32 v53, v53, v54
	v_cmp_gt_i32_e32 vcc, 0x100, v53
	s_nop 0
	s_nop 0
	v_cndmask_b32_e64 v55, 0, -1, vcc
	v_cndmask_b32_e32 v14, v14, v52, vcc
	v_bitop3_b32 v12, v12, v50, v55 bitop3:0xf8
	v_bitop3_b32 v13, v13, v51, v55 bitop3:0xf8
	v_bitop3_b32 v10, v10, v78, v55 bitop3:0x60
	v_bitop3_b32 v11, v11, v110, v55 bitop3:0x60
.Lmy_s2_p5:
	v_and_b32_e32 v50, v10, v79
	v_and_b32_e32 v51, v11, v111
	v_bcnt_u32_b32 v52, v50, v14
	v_bcnt_u32_b32 v52, v51, v52
	s_nop 1
	v_add_u32_dpp v53, v52, v52 quad_perm:[1,0,3,2] row_mask:0xf bank_mask:0xf bound_ctrl:1
	s_nop 1
	v_add_u32_dpp v53, v53, v53 quad_perm:[2,3,0,1] row_mask:0xf bank_mask:0xf bound_ctrl:1
	s_nop 1
	v_add_u32_dpp v53, v53, v53 row_half_mirror row_mask:0xf bank_mask:0xf bound_ctrl:1
	s_nop 1
	v_add_u32_dpp v53, v53, v53 row_mirror row_mask:0xf bank_mask:0xf bound_ctrl:1
	v_mov_b32_e32 v54, v53
	s_nop 1
	v_permlane16_swap_b32 v53, v54
	v_add_u32_e32 v53, v53, v54
	v_cmp_gt_i32_e32 vcc, 0x100, v53
	s_nop 0
	s_nop 0
	v_cndmask_b32_e64 v55, 0, -1, vcc
	v_cndmask_b32_e32 v14, v14, v52, vcc
	v_bitop3_b32 v12, v12, v50, v55 bitop3:0xf8
	v_bitop3_b32 v13, v13, v51, v55 bitop3:0xf8
	v_bitop3_b32 v10, v10, v79, v55 bitop3:0x60
	v_bitop3_b32 v11, v11, v111, v55 bitop3:0x60
.Lmy_s2_p6:
	v_and_b32_e32 v50, v10, v80
	v_and_b32_e32 v51, v11, v112
	v_bcnt_u32_b32 v52, v50, v14
	v_bcnt_u32_b32 v52, v51, v52
	s_nop 1
	v_add_u32_dpp v53, v52, v52 quad_perm:[1,0,3,2] row_mask:0xf bank_mask:0xf bound_ctrl:1
	s_nop 1
	v_add_u32_dpp v53, v53, v53 quad_perm:[2,3,0,1] row_mask:0xf bank_mask:0xf bound_ctrl:1
	s_nop 1
	v_add_u32_dpp v53, v53, v53 row_half_mirror row_mask:0xf bank_mask:0xf bound_ctrl:1
	s_nop 1
	v_add_u32_dpp v53, v53, v53 row_mirror row_mask:0xf bank_mask:0xf bound_ctrl:1
	v_mov_b32_e32 v54, v53
	s_nop 1
	v_permlane16_swap_b32 v53, v54
	v_add_u32_e32 v53, v53, v54
	v_cmp_gt_i32_e32 vcc, 0x100, v53
	s_nop 0
	s_nop 0
	v_cndmask_b32_e64 v55, 0, -1, vcc
	v_cndmask_b32_e32 v14, v14, v52, vcc
	v_bitop3_b32 v12, v12, v50, v55 bitop3:0xf8
	v_bitop3_b32 v13, v13, v51, v55 bitop3:0xf8
	v_bitop3_b32 v10, v10, v80, v55 bitop3:0x60
	v_bitop3_b32 v11, v11, v112, v55 bitop3:0x60
.Lmy_s2_p7:
	v_and_b32_e32 v50, v10, v81
	v_and_b32_e32 v51, v11, v113
	v_bcnt_u32_b32 v52, v50, v14
	v_bcnt_u32_b32 v52, v51, v52
	s_nop 1
	v_add_u32_dpp v53, v52, v52 quad_perm:[1,0,3,2] row_mask:0xf bank_mask:0xf bound_ctrl:1
	s_nop 1
	v_add_u32_dpp v53, v53, v53 quad_perm:[2,3,0,1] row_mask:0xf bank_mask:0xf bound_ctrl:1
	s_nop 1
	v_add_u32_dpp v53, v53, v53 row_half_mirror row_mask:0xf bank_mask:0xf bound_ctrl:1
	s_nop 1
	v_add_u32_dpp v53, v53, v53 row_mirror row_mask:0xf bank_mask:0xf bound_ctrl:1
	v_mov_b32_e32 v54, v53
	s_nop 1
	v_permlane16_swap_b32 v53, v54
	v_add_u32_e32 v53, v53, v54
	v_cmp_gt_i32_e32 vcc, 0x100, v53
	s_nop 0
	s_nop 0
	v_cndmask_b32_e64 v55, 0, -1, vcc
	v_cndmask_b32_e32 v14, v14, v52, vcc
	v_bitop3_b32 v12, v12, v50, v55 bitop3:0xf8
	v_bitop3_b32 v13, v13, v51, v55 bitop3:0xf8
	v_bitop3_b32 v10, v10, v81, v55 bitop3:0x60
	v_bitop3_b32 v11, v11, v113, v55 bitop3:0x60
